# indexer unit prologue: head-weight load no longer drains vmcnt(0) before the second group of LDS-DMA loads (counted vmcnt(4) after them); on top of hand-written posts, prologue de-waterfall, stick-bre
# speedup vs baseline: 1.0063x; 1.0000x over previous
.LBB0_699:
	s_mov_b32 s98, 0
	s_lshl_b32 s4, s37, 12
	s_and_b32 s20, s4, 0x7000
	v_add_u32_e32 v0, s20, v124
	v_ashrrev_i32_e32 v1, 31, v0
	v_readlane_b32 s4, v252, 52
	v_lshlrev_b64 v[0:1], 8, v[0:1]
	s_add_i32 s35, s4, 0
	v_lshl_add_u64 v[122:123], v[114:115], 0, v[0:1]
	s_add_i32 m0, s35, 0x10400
	s_mov_b64 s[4:5], 0x2000
	s_barrier
	global_load_lds_dwordx4 v[122:123], off
	v_lshl_add_u64 v[0:1], v[122:123], 0, s[4:5]
	s_add_i32 m0, s35, 0x12400
	s_mov_b64 s[4:5], 0x4000
	global_load_lds_dwordx4 v[0:1], off
	v_lshl_add_u64 v[0:1], v[122:123], 0, s[4:5]
	s_add_i32 m0, s35, 0x14400
	s_mov_b64 s[4:5], 0x6000
	global_load_lds_dwordx4 v[0:1], off
	v_lshl_add_u64 v[0:1], v[122:123], 0, s[4:5]
	s_add_i32 m0, s35, 0x16400
	s_waitcnt lgkmcnt(0)
	s_and_b32 s46, s37, -8
	global_load_lds_dwordx4 v[0:1], off
	s_add_i32 s20, s20, s46
	s_and_saveexec_b64 s[4:5], s[6:7]
	s_cbranch_execz .LBB0_701
	v_add_u32_e32 v0, s20, v137
	v_ashrrev_i32_e32 v1, 31, v0
	v_lshlrev_b64 v[0:1], 6, v[0:1]
	v_lshl_add_u64 v[0:1], v[120:121], 0, v[0:1]
	global_load_dword v219, v[0:1], off
.LBB0_701:
	s_or_b64 exec, exec, s[4:5]
	v_or_b32_e32 v0, s20, v125
	v_ashrrev_i32_e32 v1, 31, v0
	v_lshlrev_b64 v[0:1], 12, v[0:1]
	s_add_i32 s41, s35, 0x18400
	v_lshl_add_u64 v[0:1], v[116:117], 0, v[0:1]
	s_mov_b32 m0, s41
	s_mov_b64 s[4:5], 0x2000
	s_add_i32 s31, s35, 0x1a400
	global_load_lds_dwordx4 v[0:1], off
	v_lshl_add_u64 v[2:3], v[0:1], 0, s[4:5]
	s_mov_b32 m0, s31
	s_mov_b64 s[4:5], 0x4000
	s_add_i32 s34, s35, 0x1c400
	global_load_lds_dwordx4 v[2:3], off
	v_lshl_add_u64 v[2:3], v[0:1], 0, s[4:5]
	s_mov_b32 m0, s34
	s_mov_b64 s[4:5], 0x6000
	s_add_i32 s35, s35, 0x1e400
	global_load_lds_dwordx4 v[2:3], off
	v_lshl_add_u64 v[0:1], v[0:1], 0, s[4:5]
	s_mov_b32 m0, s35
	s_add_i32 s4, s46, 39
	global_load_lds_dwordx4 v[0:1], off
	s_and_saveexec_b64 s[56:57], s[6:7]
	s_waitcnt vmcnt(4)
	ds_write_b32 v138, v219
	s_mov_b64 exec, s[56:57]
	s_ashr_i32 s21, s4, 5
	s_add_i32 s4, s21, 3
	s_ashr_i32 s30, s4, 2
	s_cmp_lt_i32 s30, 1
	s_cbranch_scc1 .LBB0_713
	s_waitcnt vmcnt(0) lgkmcnt(0)
	s_barrier
	v_add_u32_e32 v0, v126, v128
	v_add_u32_e32 v1, v126, v129
	v_add_u32_e32 v2, v126, v130
	v_add_u32_e32 v3, v126, v131
	v_add_u32_e32 v4, v126, v132
	v_add_u32_e32 v5, v126, v133
	v_add_u32_e32 v6, v126, v134
	v_add_u32_e32 v7, v126, v135
	ds_read_b128 v[16:19], v0
	ds_read_b128 v[20:23], v0 offset:8192
	ds_read_b128 v[24:27], v1
	ds_read_b128 v[28:31], v1 offset:8192
	ds_read_b128 v[32:35], v2
	ds_read_b128 v[36:39], v2 offset:8192
	ds_read_b128 v[40:43], v3
	ds_read_b128 v[44:47], v3 offset:8192
	ds_read_b128 v[48:51], v4
	ds_read_b128 v[52:55], v4 offset:8192
	ds_read_b128 v[56:59], v5
	ds_read_b128 v[60:63], v5 offset:8192
	ds_read_b128 v[64:67], v6
	ds_read_b128 v[68:71], v6 offset:8192
	ds_read_b128 v[72:75], v7
	ds_read_b128 v[76:79], v7 offset:8192
	s_waitcnt lgkmcnt(0)
	s_barrier
	s_cmp_lg_u32 s30, 1
	s_cselect_b64 s[4:5], -1, 0
	s_cmp_eq_u32 s30, 1
	s_cbranch_scc1 .LBB0_704
	s_mov_b64 s[56:57], 0xe000
	v_lshl_add_u64 v[0:1], v[122:123], 0, s[56:57]
	s_mov_b64 s[56:57], 0xc000
	v_lshl_add_u64 v[2:3], v[122:123], 0, s[56:57]
	s_mov_b64 s[56:57], 0xa000
	v_lshl_add_u64 v[4:5], v[122:123], 0, s[56:57]
	s_mov_b64 s[56:57], 0x8000
	s_mov_b32 m0, s41
	v_lshl_add_u64 v[6:7], v[122:123], 0, s[56:57]
	global_load_lds_dwordx4 v[6:7], off
	s_mov_b32 m0, s31
	s_nop 0
	global_load_lds_dwordx4 v[4:5], off
	s_mov_b32 m0, s34
	s_nop 0
	global_load_lds_dwordx4 v[2:3], off
	s_mov_b32 m0, s35
	s_nop 0
	global_load_lds_dwordx4 v[0:1], off
